# g7: g5 + P6 gate-up epilogue regenerated (9 instead of 11 VALU per output: folded exp2 constant, packed +1.0)
# speedup vs baseline: 1.0109x; 1.0078x over previous
.LBB0_614:
	s_nop 15
	s_nop 15
	v_add_u32_e32 v2, s65, v185
	ds_read_b128 v[14:17], v2
	ds_read_b128 v[10:13], v2 offset:16
	ds_read_b128 v[6:9], v2 offset:32
	ds_read_b128 v[2:5], v2 offset:48
	v_lshl_add_u32 v20, s64, 8, v184
	s_waitcnt lgkmcnt(0)
	v_mov_b32_e32 v226, 1.0
	v_mov_b32_e32 v227, 1.0
	v_pk_add_f32 v[158:159], v[158:159], v[14:15]
	v_pk_add_f32 v[160:161], v[160:161], v[16:17]
	v_pk_add_f32 v[154:155], v[154:155], v[10:11]
	v_pk_add_f32 v[156:157], v[156:157], v[12:13]
	v_pk_add_f32 v[150:151], v[150:151], v[6:7]
	v_pk_add_f32 v[152:153], v[152:153], v[8:9]
	v_pk_add_f32 v[146:147], v[146:147], v[2:3]
	v_pk_add_f32 v[148:149], v[148:149], v[4:5]
	v_min_f32_e32 v158, 0x40e00000, v158
	v_min_f32_e32 v160, 0x40e00000, v160
	v_min_f32_e32 v154, 0x40e00000, v154
	v_min_f32_e32 v156, 0x40e00000, v156
	v_min_f32_e32 v150, 0x40e00000, v150
	v_min_f32_e32 v152, 0x40e00000, v152
	v_min_f32_e32 v146, 0x40e00000, v146
	v_min_f32_e32 v148, 0x40e00000, v148
	v_mul_f32_e32 v206, 0xc01d265f, v158
	v_mul_f32_e32 v208, 0xc01d265f, v160
	v_mul_f32_e32 v210, 0xc01d265f, v154
	v_mul_f32_e32 v212, 0xc01d265f, v156
	v_mul_f32_e32 v214, 0xc01d265f, v150
	v_mul_f32_e32 v216, 0xc01d265f, v152
	v_mul_f32_e32 v218, 0xc01d265f, v146
	v_mul_f32_e32 v220, 0xc01d265f, v148
	v_exp_f32_e32 v206, v206
	v_exp_f32_e32 v208, v208
	v_exp_f32_e32 v210, v210
	v_exp_f32_e32 v212, v212
	v_exp_f32_e32 v214, v214
	v_exp_f32_e32 v216, v216
	v_exp_f32_e32 v218, v218
	v_exp_f32_e32 v220, v220
	v_med3_f32 v207, v159, s58, v195
	v_med3_f32 v209, v161, s58, v195
	v_med3_f32 v211, v155, s58, v195
	v_med3_f32 v213, v157, s58, v195
	v_med3_f32 v215, v151, s58, v195
	v_med3_f32 v217, v153, s58, v195
	v_med3_f32 v219, v147, s58, v195
	v_med3_f32 v221, v149, s58, v195
	v_pk_add_f32 v[206:207], v[206:207], v[226:227]
	v_pk_add_f32 v[208:209], v[208:209], v[226:227]
	v_pk_add_f32 v[210:211], v[210:211], v[226:227]
	v_pk_add_f32 v[212:213], v[212:213], v[226:227]
	v_pk_add_f32 v[214:215], v[214:215], v[226:227]
	v_pk_add_f32 v[216:217], v[216:217], v[226:227]
	v_pk_add_f32 v[218:219], v[218:219], v[226:227]
	v_pk_add_f32 v[220:221], v[220:221], v[226:227]
	v_rcp_f32_e32 v206, v206
	v_rcp_f32_e32 v208, v208
	v_rcp_f32_e32 v210, v210
	v_rcp_f32_e32 v212, v212
	v_rcp_f32_e32 v214, v214
	v_rcp_f32_e32 v216, v216
	v_rcp_f32_e32 v218, v218
	v_rcp_f32_e32 v220, v220
	v_mul_f32_e32 v158, v158, v206
	v_mul_f32_e32 v160, v160, v208
	v_mul_f32_e32 v154, v154, v210
	v_mul_f32_e32 v156, v156, v212
	v_mul_f32_e32 v150, v150, v214
	v_mul_f32_e32 v152, v152, v216
	v_mul_f32_e32 v146, v146, v218
	v_mul_f32_e32 v148, v148, v220
	v_mul_f32_e32 v158, v207, v158
	v_mul_f32_e32 v160, v209, v160
	v_mul_f32_e32 v154, v211, v154
	v_mul_f32_e32 v156, v213, v156
	v_mul_f32_e32 v150, v215, v150
	v_mul_f32_e32 v152, v217, v152
	v_mul_f32_e32 v146, v219, v146
	v_mul_f32_e32 v148, v221, v148
	v_cvt_pk_fp8_f32 v222, v158, v160
	v_cvt_pk_fp8_f32 v223, v150, v152
	s_lshl_b32 s4, s38, 7
	v_ashrrev_i32_e32 v21, 31, v20
	s_and_b32 s4, s4, 0x780
	v_lshlrev_b64 v[18:19], 11, v[20:21]
	v_or_b32_e32 v168, s4, v183
	v_lshl_add_u64 v[18:19], s[14:15], 0, v[18:19]
	v_lshl_add_u64 v[18:19], v[18:19], 0, v[168:169]
	v_cvt_pk_fp8_f32 v222, v154, v156 op_sel:[0,0,1]
	v_cvt_pk_fp8_f32 v223, v146, v148 op_sel:[0,0,1]
	global_store_dwordx2 v[18:19], v[222:223], off
	v_pk_add_f32 v[142:143], v[142:143], v[14:15]
	v_pk_add_f32 v[144:145], v[144:145], v[16:17]
	v_pk_add_f32 v[138:139], v[138:139], v[10:11]
	v_pk_add_f32 v[140:141], v[140:141], v[12:13]
	v_pk_add_f32 v[134:135], v[134:135], v[6:7]
	v_pk_add_f32 v[136:137], v[136:137], v[8:9]
	v_pk_add_f32 v[130:131], v[130:131], v[2:3]
	v_pk_add_f32 v[132:133], v[132:133], v[4:5]
	v_min_f32_e32 v142, 0x40e00000, v142
	v_min_f32_e32 v144, 0x40e00000, v144
	v_min_f32_e32 v138, 0x40e00000, v138
	v_min_f32_e32 v140, 0x40e00000, v140
	v_min_f32_e32 v134, 0x40e00000, v134
	v_min_f32_e32 v136, 0x40e00000, v136
	v_min_f32_e32 v130, 0x40e00000, v130
	v_min_f32_e32 v132, 0x40e00000, v132
	v_mul_f32_e32 v206, 0xc01d265f, v142
	v_mul_f32_e32 v208, 0xc01d265f, v144
	v_mul_f32_e32 v210, 0xc01d265f, v138
	v_mul_f32_e32 v212, 0xc01d265f, v140
	v_mul_f32_e32 v214, 0xc01d265f, v134
	v_mul_f32_e32 v216, 0xc01d265f, v136
	v_mul_f32_e32 v218, 0xc01d265f, v130
	v_mul_f32_e32 v220, 0xc01d265f, v132
	v_exp_f32_e32 v206, v206
	v_exp_f32_e32 v208, v208
	v_exp_f32_e32 v210, v210
	v_exp_f32_e32 v212, v212
	v_exp_f32_e32 v214, v214
	v_exp_f32_e32 v216, v216
	v_exp_f32_e32 v218, v218
	v_exp_f32_e32 v220, v220
	v_med3_f32 v207, v143, s58, v195
	v_med3_f32 v209, v145, s58, v195
	v_med3_f32 v211, v139, s58, v195
	v_med3_f32 v213, v141, s58, v195
	v_med3_f32 v215, v135, s58, v195
	v_med3_f32 v217, v137, s58, v195
	v_med3_f32 v219, v131, s58, v195
	v_med3_f32 v221, v133, s58, v195
	v_pk_add_f32 v[206:207], v[206:207], v[226:227]
	v_pk_add_f32 v[208:209], v[208:209], v[226:227]
	v_pk_add_f32 v[210:211], v[210:211], v[226:227]
	v_pk_add_f32 v[212:213], v[212:213], v[226:227]
	v_pk_add_f32 v[214:215], v[214:215], v[226:227]
	v_pk_add_f32 v[216:217], v[216:217], v[226:227]
	v_pk_add_f32 v[218:219], v[218:219], v[226:227]
	v_pk_add_f32 v[220:221], v[220:221], v[226:227]
	v_rcp_f32_e32 v206, v206
	v_rcp_f32_e32 v208, v208
	v_rcp_f32_e32 v210, v210
	v_rcp_f32_e32 v212, v212
	v_rcp_f32_e32 v214, v214
	v_rcp_f32_e32 v216, v216
	v_rcp_f32_e32 v218, v218
	v_rcp_f32_e32 v220, v220
	v_mul_f32_e32 v142, v142, v206
	v_mul_f32_e32 v144, v144, v208
	v_mul_f32_e32 v138, v138, v210
	v_mul_f32_e32 v140, v140, v212
	v_mul_f32_e32 v134, v134, v214
	v_mul_f32_e32 v136, v136, v216
	v_mul_f32_e32 v130, v130, v218
	v_mul_f32_e32 v132, v132, v220
	v_mul_f32_e32 v142, v207, v142
	v_mul_f32_e32 v144, v209, v144
	v_mul_f32_e32 v138, v211, v138
	v_mul_f32_e32 v140, v213, v140
	v_mul_f32_e32 v134, v215, v134
	v_mul_f32_e32 v136, v217, v136
	v_mul_f32_e32 v130, v219, v130
	v_mul_f32_e32 v132, v221, v132
	v_cvt_pk_fp8_f32 v222, v142, v144
	v_cvt_pk_fp8_f32 v223, v134, v136
	v_or_b32_e32 v224, 16, v20
	v_ashrrev_i32_e32 v225, 31, v224
	v_lshlrev_b64 v[224:225], 11, v[224:225]
	v_lshl_add_u64 v[224:225], s[14:15], 0, v[224:225]
	v_lshl_add_u64 v[224:225], v[224:225], 0, v[168:169]
	v_cvt_pk_fp8_f32 v222, v138, v140 op_sel:[0,0,1]
	v_cvt_pk_fp8_f32 v223, v130, v132 op_sel:[0,0,1]
	global_store_dwordx2 v[224:225], v[222:223], off
	v_pk_add_f32 v[126:127], v[126:127], v[14:15]
	v_pk_add_f32 v[128:129], v[128:129], v[16:17]
	v_pk_add_f32 v[122:123], v[122:123], v[10:11]
	v_pk_add_f32 v[124:125], v[124:125], v[12:13]
	v_pk_add_f32 v[118:119], v[118:119], v[6:7]
	v_pk_add_f32 v[120:121], v[120:121], v[8:9]
	v_pk_add_f32 v[114:115], v[114:115], v[2:3]
	v_pk_add_f32 v[116:117], v[116:117], v[4:5]
	v_min_f32_e32 v126, 0x40e00000, v126
	v_min_f32_e32 v128, 0x40e00000, v128
	v_min_f32_e32 v122, 0x40e00000, v122
	v_min_f32_e32 v124, 0x40e00000, v124
	v_min_f32_e32 v118, 0x40e00000, v118
	v_min_f32_e32 v120, 0x40e00000, v120
	v_min_f32_e32 v114, 0x40e00000, v114
	v_min_f32_e32 v116, 0x40e00000, v116
	v_mul_f32_e32 v206, 0xc01d265f, v126
	v_mul_f32_e32 v208, 0xc01d265f, v128
	v_mul_f32_e32 v210, 0xc01d265f, v122
	v_mul_f32_e32 v212, 0xc01d265f, v124
	v_mul_f32_e32 v214, 0xc01d265f, v118
	v_mul_f32_e32 v216, 0xc01d265f, v120
	v_mul_f32_e32 v218, 0xc01d265f, v114
	v_mul_f32_e32 v220, 0xc01d265f, v116
	v_exp_f32_e32 v206, v206
	v_exp_f32_e32 v208, v208
	v_exp_f32_e32 v210, v210
	v_exp_f32_e32 v212, v212
	v_exp_f32_e32 v214, v214
	v_exp_f32_e32 v216, v216
	v_exp_f32_e32 v218, v218
	v_exp_f32_e32 v220, v220
	v_med3_f32 v207, v127, s58, v195
	v_med3_f32 v209, v129, s58, v195
	v_med3_f32 v211, v123, s58, v195
	v_med3_f32 v213, v125, s58, v195
	v_med3_f32 v215, v119, s58, v195
	v_med3_f32 v217, v121, s58, v195
	v_med3_f32 v219, v115, s58, v195
	v_med3_f32 v221, v117, s58, v195
	v_pk_add_f32 v[206:207], v[206:207], v[226:227]
	v_pk_add_f32 v[208:209], v[208:209], v[226:227]
	v_pk_add_f32 v[210:211], v[210:211], v[226:227]
	v_pk_add_f32 v[212:213], v[212:213], v[226:227]
	v_pk_add_f32 v[214:215], v[214:215], v[226:227]
	v_pk_add_f32 v[216:217], v[216:217], v[226:227]
	v_pk_add_f32 v[218:219], v[218:219], v[226:227]
	v_pk_add_f32 v[220:221], v[220:221], v[226:227]
	v_rcp_f32_e32 v206, v206
	v_rcp_f32_e32 v208, v208
	v_rcp_f32_e32 v210, v210
	v_rcp_f32_e32 v212, v212
	v_rcp_f32_e32 v214, v214
	v_rcp_f32_e32 v216, v216
	v_rcp_f32_e32 v218, v218
	v_rcp_f32_e32 v220, v220
	v_mul_f32_e32 v126, v126, v206
	v_mul_f32_e32 v128, v128, v208
	v_mul_f32_e32 v122, v122, v210
	v_mul_f32_e32 v124, v124, v212
	v_mul_f32_e32 v118, v118, v214
	v_mul_f32_e32 v120, v120, v216
	v_mul_f32_e32 v114, v114, v218
	v_mul_f32_e32 v116, v116, v220
	v_mul_f32_e32 v126, v207, v126
	v_mul_f32_e32 v128, v209, v128
	v_mul_f32_e32 v122, v211, v122
	v_mul_f32_e32 v124, v213, v124
	v_mul_f32_e32 v118, v215, v118
	v_mul_f32_e32 v120, v217, v120
	v_mul_f32_e32 v114, v219, v114
	v_mul_f32_e32 v116, v221, v116
	v_cvt_pk_fp8_f32 v222, v126, v128
	v_cvt_pk_fp8_f32 v223, v118, v120
	v_or_b32_e32 v224, 32, v20
	v_ashrrev_i32_e32 v225, 31, v224
	v_lshlrev_b64 v[224:225], 11, v[224:225]
	v_lshl_add_u64 v[224:225], s[14:15], 0, v[224:225]
	v_lshl_add_u64 v[224:225], v[224:225], 0, v[168:169]
	v_cvt_pk_fp8_f32 v222, v122, v124 op_sel:[0,0,1]
	v_cvt_pk_fp8_f32 v223, v114, v116 op_sel:[0,0,1]
	global_store_dwordx2 v[224:225], v[222:223], off
	v_pk_add_f32 v[110:111], v[110:111], v[14:15]
	v_pk_add_f32 v[112:113], v[112:113], v[16:17]
	v_pk_add_f32 v[106:107], v[106:107], v[10:11]
	v_pk_add_f32 v[108:109], v[108:109], v[12:13]
	v_pk_add_f32 v[98:99], v[98:99], v[6:7]
	v_pk_add_f32 v[100:101], v[100:101], v[8:9]
	v_pk_add_f32 v[90:91], v[90:91], v[2:3]
	v_pk_add_f32 v[92:93], v[92:93], v[4:5]
	v_min_f32_e32 v110, 0x40e00000, v110
	v_min_f32_e32 v112, 0x40e00000, v112
	v_min_f32_e32 v106, 0x40e00000, v106
	v_min_f32_e32 v108, 0x40e00000, v108
	v_min_f32_e32 v98, 0x40e00000, v98
	v_min_f32_e32 v100, 0x40e00000, v100
	v_min_f32_e32 v90, 0x40e00000, v90
	v_min_f32_e32 v92, 0x40e00000, v92
	v_mul_f32_e32 v206, 0xc01d265f, v110
	v_mul_f32_e32 v208, 0xc01d265f, v112
	v_mul_f32_e32 v210, 0xc01d265f, v106
	v_mul_f32_e32 v212, 0xc01d265f, v108
	v_mul_f32_e32 v214, 0xc01d265f, v98
	v_mul_f32_e32 v216, 0xc01d265f, v100
	v_mul_f32_e32 v218, 0xc01d265f, v90
	v_mul_f32_e32 v220, 0xc01d265f, v92
	v_exp_f32_e32 v206, v206
	v_exp_f32_e32 v208, v208
	v_exp_f32_e32 v210, v210
	v_exp_f32_e32 v212, v212
	v_exp_f32_e32 v214, v214
	v_exp_f32_e32 v216, v216
	v_exp_f32_e32 v218, v218
	v_exp_f32_e32 v220, v220
	v_med3_f32 v207, v111, s58, v195
	v_med3_f32 v209, v113, s58, v195
	v_med3_f32 v211, v107, s58, v195
	v_med3_f32 v213, v109, s58, v195
	v_med3_f32 v215, v99, s58, v195
	v_med3_f32 v217, v101, s58, v195
	v_med3_f32 v219, v91, s58, v195
	v_med3_f32 v221, v93, s58, v195
	v_pk_add_f32 v[206:207], v[206:207], v[226:227]
	v_pk_add_f32 v[208:209], v[208:209], v[226:227]
	v_pk_add_f32 v[210:211], v[210:211], v[226:227]
	v_pk_add_f32 v[212:213], v[212:213], v[226:227]
	v_pk_add_f32 v[214:215], v[214:215], v[226:227]
	v_pk_add_f32 v[216:217], v[216:217], v[226:227]
	v_pk_add_f32 v[218:219], v[218:219], v[226:227]
	v_pk_add_f32 v[220:221], v[220:221], v[226:227]
	v_rcp_f32_e32 v206, v206
	v_rcp_f32_e32 v208, v208
	v_rcp_f32_e32 v210, v210
	v_rcp_f32_e32 v212, v212
	v_rcp_f32_e32 v214, v214
	v_rcp_f32_e32 v216, v216
	v_rcp_f32_e32 v218, v218
	v_rcp_f32_e32 v220, v220
	v_mul_f32_e32 v110, v110, v206
	v_mul_f32_e32 v112, v112, v208
	v_mul_f32_e32 v106, v106, v210
	v_mul_f32_e32 v108, v108, v212
	v_mul_f32_e32 v98, v98, v214
	v_mul_f32_e32 v100, v100, v216
	v_mul_f32_e32 v90, v90, v218
	v_mul_f32_e32 v92, v92, v220
	v_mul_f32_e32 v110, v207, v110
	v_mul_f32_e32 v112, v209, v112
	v_mul_f32_e32 v106, v211, v106
	v_mul_f32_e32 v108, v213, v108
	v_mul_f32_e32 v98, v215, v98
	v_mul_f32_e32 v100, v217, v100
	v_mul_f32_e32 v90, v219, v90
	v_mul_f32_e32 v92, v221, v92
	v_cvt_pk_fp8_f32 v222, v110, v112
	v_cvt_pk_fp8_f32 v223, v98, v100
	v_or_b32_e32 v224, 48, v20
	v_ashrrev_i32_e32 v225, 31, v224
	v_lshlrev_b64 v[224:225], 11, v[224:225]
	v_lshl_add_u64 v[224:225], s[14:15], 0, v[224:225]
	v_lshl_add_u64 v[224:225], v[224:225], 0, v[168:169]
	v_cvt_pk_fp8_f32 v222, v106, v108 op_sel:[0,0,1]
	v_cvt_pk_fp8_f32 v223, v90, v92 op_sel:[0,0,1]
	global_store_dwordx2 v[224:225], v[222:223], off
	v_pk_add_f32 v[102:103], v[102:103], v[14:15]
	v_pk_add_f32 v[104:105], v[104:105], v[16:17]
	v_pk_add_f32 v[94:95], v[94:95], v[10:11]
	v_pk_add_f32 v[96:97], v[96:97], v[12:13]
	v_pk_add_f32 v[86:87], v[86:87], v[6:7]
	v_pk_add_f32 v[88:89], v[88:89], v[8:9]
	v_pk_add_f32 v[82:83], v[82:83], v[2:3]
	v_pk_add_f32 v[84:85], v[84:85], v[4:5]
	v_min_f32_e32 v102, 0x40e00000, v102
	v_min_f32_e32 v104, 0x40e00000, v104
	v_min_f32_e32 v94, 0x40e00000, v94
	v_min_f32_e32 v96, 0x40e00000, v96
	v_min_f32_e32 v86, 0x40e00000, v86
	v_min_f32_e32 v88, 0x40e00000, v88
	v_min_f32_e32 v82, 0x40e00000, v82
	v_min_f32_e32 v84, 0x40e00000, v84
	v_mul_f32_e32 v206, 0xc01d265f, v102
	v_mul_f32_e32 v208, 0xc01d265f, v104
	v_mul_f32_e32 v210, 0xc01d265f, v94
	v_mul_f32_e32 v212, 0xc01d265f, v96
	v_mul_f32_e32 v214, 0xc01d265f, v86
	v_mul_f32_e32 v216, 0xc01d265f, v88
	v_mul_f32_e32 v218, 0xc01d265f, v82
	v_mul_f32_e32 v220, 0xc01d265f, v84
	v_exp_f32_e32 v206, v206
	v_exp_f32_e32 v208, v208
	v_exp_f32_e32 v210, v210
	v_exp_f32_e32 v212, v212
	v_exp_f32_e32 v214, v214
	v_exp_f32_e32 v216, v216
	v_exp_f32_e32 v218, v218
	v_exp_f32_e32 v220, v220
	v_med3_f32 v207, v103, s58, v195
	v_med3_f32 v209, v105, s58, v195
	v_med3_f32 v211, v95, s58, v195
	v_med3_f32 v213, v97, s58, v195
	v_med3_f32 v215, v87, s58, v195
	v_med3_f32 v217, v89, s58, v195
	v_med3_f32 v219, v83, s58, v195
	v_med3_f32 v221, v85, s58, v195
	v_pk_add_f32 v[206:207], v[206:207], v[226:227]
	v_pk_add_f32 v[208:209], v[208:209], v[226:227]
	v_pk_add_f32 v[210:211], v[210:211], v[226:227]
	v_pk_add_f32 v[212:213], v[212:213], v[226:227]
	v_pk_add_f32 v[214:215], v[214:215], v[226:227]
	v_pk_add_f32 v[216:217], v[216:217], v[226:227]
	v_pk_add_f32 v[218:219], v[218:219], v[226:227]
	v_pk_add_f32 v[220:221], v[220:221], v[226:227]
	v_rcp_f32_e32 v206, v206
	v_rcp_f32_e32 v208, v208
	v_rcp_f32_e32 v210, v210
	v_rcp_f32_e32 v212, v212
	v_rcp_f32_e32 v214, v214
	v_rcp_f32_e32 v216, v216
	v_rcp_f32_e32 v218, v218
	v_rcp_f32_e32 v220, v220
	v_mul_f32_e32 v102, v102, v206
	v_mul_f32_e32 v104, v104, v208
	v_mul_f32_e32 v94, v94, v210
	v_mul_f32_e32 v96, v96, v212
	v_mul_f32_e32 v86, v86, v214
	v_mul_f32_e32 v88, v88, v216
	v_mul_f32_e32 v82, v82, v218
	v_mul_f32_e32 v84, v84, v220
	v_mul_f32_e32 v102, v207, v102
	v_mul_f32_e32 v104, v209, v104
	v_mul_f32_e32 v94, v211, v94
	v_mul_f32_e32 v96, v213, v96
	v_mul_f32_e32 v86, v215, v86
	v_mul_f32_e32 v88, v217, v88
	v_mul_f32_e32 v82, v219, v82
	v_mul_f32_e32 v84, v221, v84
	v_cvt_pk_fp8_f32 v222, v102, v104
	v_cvt_pk_fp8_f32 v223, v86, v88
	v_add_co_u32_e32 v224, vcc, s59, v18
	s_nop 1
	v_addc_co_u32_e32 v225, vcc, 0, v19, vcc
	v_cvt_pk_fp8_f32 v222, v94, v96 op_sel:[0,0,1]
	v_cvt_pk_fp8_f32 v223, v82, v84 op_sel:[0,0,1]
	global_store_dwordx2 v[224:225], v[222:223], off
	v_pk_add_f32 v[78:79], v[78:79], v[14:15]
	v_pk_add_f32 v[80:81], v[80:81], v[16:17]
	v_pk_add_f32 v[74:75], v[74:75], v[10:11]
	v_pk_add_f32 v[76:77], v[76:77], v[12:13]
	v_pk_add_f32 v[70:71], v[70:71], v[6:7]
	v_pk_add_f32 v[72:73], v[72:73], v[8:9]
	v_pk_add_f32 v[66:67], v[66:67], v[2:3]
	v_pk_add_f32 v[68:69], v[68:69], v[4:5]
	v_min_f32_e32 v78, 0x40e00000, v78
	v_min_f32_e32 v80, 0x40e00000, v80
	v_min_f32_e32 v74, 0x40e00000, v74
	v_min_f32_e32 v76, 0x40e00000, v76
	v_min_f32_e32 v70, 0x40e00000, v70
	v_min_f32_e32 v72, 0x40e00000, v72
	v_min_f32_e32 v66, 0x40e00000, v66
	v_min_f32_e32 v68, 0x40e00000, v68
	v_mul_f32_e32 v206, 0xc01d265f, v78
	v_mul_f32_e32 v208, 0xc01d265f, v80
	v_mul_f32_e32 v210, 0xc01d265f, v74
	v_mul_f32_e32 v212, 0xc01d265f, v76
	v_mul_f32_e32 v214, 0xc01d265f, v70
	v_mul_f32_e32 v216, 0xc01d265f, v72
	v_mul_f32_e32 v218, 0xc01d265f, v66
	v_mul_f32_e32 v220, 0xc01d265f, v68
	v_exp_f32_e32 v206, v206
	v_exp_f32_e32 v208, v208
	v_exp_f32_e32 v210, v210
	v_exp_f32_e32 v212, v212
	v_exp_f32_e32 v214, v214
	v_exp_f32_e32 v216, v216
	v_exp_f32_e32 v218, v218
	v_exp_f32_e32 v220, v220
	v_med3_f32 v207, v79, s58, v195
	v_med3_f32 v209, v81, s58, v195
	v_med3_f32 v211, v75, s58, v195
	v_med3_f32 v213, v77, s58, v195
	v_med3_f32 v215, v71, s58, v195
	v_med3_f32 v217, v73, s58, v195
	v_med3_f32 v219, v67, s58, v195
	v_med3_f32 v221, v69, s58, v195
	v_pk_add_f32 v[206:207], v[206:207], v[226:227]
	v_pk_add_f32 v[208:209], v[208:209], v[226:227]
	v_pk_add_f32 v[210:211], v[210:211], v[226:227]
	v_pk_add_f32 v[212:213], v[212:213], v[226:227]
	v_pk_add_f32 v[214:215], v[214:215], v[226:227]
	v_pk_add_f32 v[216:217], v[216:217], v[226:227]
	v_pk_add_f32 v[218:219], v[218:219], v[226:227]
	v_pk_add_f32 v[220:221], v[220:221], v[226:227]
	v_rcp_f32_e32 v206, v206
	v_rcp_f32_e32 v208, v208
	v_rcp_f32_e32 v210, v210
	v_rcp_f32_e32 v212, v212
	v_rcp_f32_e32 v214, v214
	v_rcp_f32_e32 v216, v216
	v_rcp_f32_e32 v218, v218
	v_rcp_f32_e32 v220, v220
	v_mul_f32_e32 v78, v78, v206
	v_mul_f32_e32 v80, v80, v208
	v_mul_f32_e32 v74, v74, v210
	v_mul_f32_e32 v76, v76, v212
	v_mul_f32_e32 v70, v70, v214
	v_mul_f32_e32 v72, v72, v216
	v_mul_f32_e32 v66, v66, v218
	v_mul_f32_e32 v68, v68, v220
	v_mul_f32_e32 v78, v207, v78
	v_mul_f32_e32 v80, v209, v80
	v_mul_f32_e32 v74, v211, v74
	v_mul_f32_e32 v76, v213, v76
	v_mul_f32_e32 v70, v215, v70
	v_mul_f32_e32 v72, v217, v72
	v_mul_f32_e32 v66, v219, v66
	v_mul_f32_e32 v68, v221, v68
	v_cvt_pk_fp8_f32 v222, v78, v80
	v_cvt_pk_fp8_f32 v223, v70, v72
	v_add_co_u32_e32 v224, vcc, s60, v18
	s_nop 1
	v_addc_co_u32_e32 v225, vcc, 0, v19, vcc
	v_cvt_pk_fp8_f32 v222, v74, v76 op_sel:[0,0,1]
	v_cvt_pk_fp8_f32 v223, v66, v68 op_sel:[0,0,1]
	global_store_dwordx2 v[224:225], v[222:223], off
	v_pk_add_f32 v[62:63], v[62:63], v[14:15]
	v_pk_add_f32 v[64:65], v[64:65], v[16:17]
	v_pk_add_f32 v[58:59], v[58:59], v[10:11]
	v_pk_add_f32 v[60:61], v[60:61], v[12:13]
	v_pk_add_f32 v[54:55], v[54:55], v[6:7]
	v_pk_add_f32 v[56:57], v[56:57], v[8:9]
	v_pk_add_f32 v[50:51], v[50:51], v[2:3]
	v_pk_add_f32 v[52:53], v[52:53], v[4:5]
	v_min_f32_e32 v62, 0x40e00000, v62
	v_min_f32_e32 v64, 0x40e00000, v64
	v_min_f32_e32 v58, 0x40e00000, v58
	v_min_f32_e32 v60, 0x40e00000, v60
	v_min_f32_e32 v54, 0x40e00000, v54
	v_min_f32_e32 v56, 0x40e00000, v56
	v_min_f32_e32 v50, 0x40e00000, v50
	v_min_f32_e32 v52, 0x40e00000, v52
	v_mul_f32_e32 v206, 0xc01d265f, v62
	v_mul_f32_e32 v208, 0xc01d265f, v64
	v_mul_f32_e32 v210, 0xc01d265f, v58
	v_mul_f32_e32 v212, 0xc01d265f, v60
	v_mul_f32_e32 v214, 0xc01d265f, v54
	v_mul_f32_e32 v216, 0xc01d265f, v56
	v_mul_f32_e32 v218, 0xc01d265f, v50
	v_mul_f32_e32 v220, 0xc01d265f, v52
	v_exp_f32_e32 v206, v206
	v_exp_f32_e32 v208, v208
	v_exp_f32_e32 v210, v210
	v_exp_f32_e32 v212, v212
	v_exp_f32_e32 v214, v214
	v_exp_f32_e32 v216, v216
	v_exp_f32_e32 v218, v218
	v_exp_f32_e32 v220, v220
	v_med3_f32 v207, v63, s58, v195
	v_med3_f32 v209, v65, s58, v195
	v_med3_f32 v211, v59, s58, v195
	v_med3_f32 v213, v61, s58, v195
	v_med3_f32 v215, v55, s58, v195
	v_med3_f32 v217, v57, s58, v195
	v_med3_f32 v219, v51, s58, v195
	v_med3_f32 v221, v53, s58, v195
	v_pk_add_f32 v[206:207], v[206:207], v[226:227]
	v_pk_add_f32 v[208:209], v[208:209], v[226:227]
	v_pk_add_f32 v[210:211], v[210:211], v[226:227]
	v_pk_add_f32 v[212:213], v[212:213], v[226:227]
	v_pk_add_f32 v[214:215], v[214:215], v[226:227]
	v_pk_add_f32 v[216:217], v[216:217], v[226:227]
	v_pk_add_f32 v[218:219], v[218:219], v[226:227]
	v_pk_add_f32 v[220:221], v[220:221], v[226:227]
	v_rcp_f32_e32 v206, v206
	v_rcp_f32_e32 v208, v208
	v_rcp_f32_e32 v210, v210
	v_rcp_f32_e32 v212, v212
	v_rcp_f32_e32 v214, v214
	v_rcp_f32_e32 v216, v216
	v_rcp_f32_e32 v218, v218
	v_rcp_f32_e32 v220, v220
	v_mul_f32_e32 v62, v62, v206
	v_mul_f32_e32 v64, v64, v208
	v_mul_f32_e32 v58, v58, v210
	v_mul_f32_e32 v60, v60, v212
	v_mul_f32_e32 v54, v54, v214
	v_mul_f32_e32 v56, v56, v216
	v_mul_f32_e32 v50, v50, v218
	v_mul_f32_e32 v52, v52, v220
	v_mul_f32_e32 v62, v207, v62
	v_mul_f32_e32 v64, v209, v64
	v_mul_f32_e32 v58, v211, v58
	v_mul_f32_e32 v60, v213, v60
	v_mul_f32_e32 v54, v215, v54
	v_mul_f32_e32 v56, v217, v56
	v_mul_f32_e32 v50, v219, v50
	v_mul_f32_e32 v52, v221, v52
	v_cvt_pk_fp8_f32 v222, v62, v64
	v_cvt_pk_fp8_f32 v223, v54, v56
	v_add_co_u32_e32 v224, vcc, s61, v18
	s_nop 1
	v_addc_co_u32_e32 v225, vcc, 0, v19, vcc
	v_cvt_pk_fp8_f32 v222, v58, v60 op_sel:[0,0,1]
	v_cvt_pk_fp8_f32 v223, v50, v52 op_sel:[0,0,1]
	global_store_dwordx2 v[224:225], v[222:223], off
	v_pk_add_f32 v[46:47], v[46:47], v[14:15]
	v_pk_add_f32 v[48:49], v[48:49], v[16:17]
	v_pk_add_f32 v[42:43], v[42:43], v[10:11]
	v_pk_add_f32 v[44:45], v[44:45], v[12:13]
	v_pk_add_f32 v[38:39], v[38:39], v[6:7]
	v_pk_add_f32 v[40:41], v[40:41], v[8:9]
	v_pk_add_f32 v[34:35], v[34:35], v[2:3]
	v_pk_add_f32 v[36:37], v[36:37], v[4:5]
	v_min_f32_e32 v46, 0x40e00000, v46
	v_min_f32_e32 v48, 0x40e00000, v48
	v_min_f32_e32 v42, 0x40e00000, v42
	v_min_f32_e32 v44, 0x40e00000, v44
	v_min_f32_e32 v38, 0x40e00000, v38
	v_min_f32_e32 v40, 0x40e00000, v40
	v_min_f32_e32 v34, 0x40e00000, v34
	v_min_f32_e32 v36, 0x40e00000, v36
	v_mul_f32_e32 v206, 0xc01d265f, v46
	v_mul_f32_e32 v208, 0xc01d265f, v48
	v_mul_f32_e32 v210, 0xc01d265f, v42
	v_mul_f32_e32 v212, 0xc01d265f, v44
	v_mul_f32_e32 v214, 0xc01d265f, v38
	v_mul_f32_e32 v216, 0xc01d265f, v40
	v_mul_f32_e32 v218, 0xc01d265f, v34
	v_mul_f32_e32 v220, 0xc01d265f, v36
	v_exp_f32_e32 v206, v206
	v_exp_f32_e32 v208, v208
	v_exp_f32_e32 v210, v210
	v_exp_f32_e32 v212, v212
	v_exp_f32_e32 v214, v214
	v_exp_f32_e32 v216, v216
	v_exp_f32_e32 v218, v218
	v_exp_f32_e32 v220, v220
	v_med3_f32 v207, v47, s58, v195
	v_med3_f32 v209, v49, s58, v195
	v_med3_f32 v211, v43, s58, v195
	v_med3_f32 v213, v45, s58, v195
	v_med3_f32 v215, v39, s58, v195
	v_med3_f32 v217, v41, s58, v195
	v_med3_f32 v219, v35, s58, v195
	v_med3_f32 v221, v37, s58, v195
	v_pk_add_f32 v[206:207], v[206:207], v[226:227]
	v_pk_add_f32 v[208:209], v[208:209], v[226:227]
	v_pk_add_f32 v[210:211], v[210:211], v[226:227]
	v_pk_add_f32 v[212:213], v[212:213], v[226:227]
	v_pk_add_f32 v[214:215], v[214:215], v[226:227]
	v_pk_add_f32 v[216:217], v[216:217], v[226:227]
	v_pk_add_f32 v[218:219], v[218:219], v[226:227]
	v_pk_add_f32 v[220:221], v[220:221], v[226:227]
	v_rcp_f32_e32 v206, v206
	v_rcp_f32_e32 v208, v208
	v_rcp_f32_e32 v210, v210
	v_rcp_f32_e32 v212, v212
	v_rcp_f32_e32 v214, v214
	v_rcp_f32_e32 v216, v216
	v_rcp_f32_e32 v218, v218
	v_rcp_f32_e32 v220, v220
	v_mul_f32_e32 v46, v46, v206
	v_mul_f32_e32 v48, v48, v208
	v_mul_f32_e32 v42, v42, v210
	v_mul_f32_e32 v44, v44, v212
	v_mul_f32_e32 v38, v38, v214
	v_mul_f32_e32 v40, v40, v216
	v_mul_f32_e32 v34, v34, v218
	v_mul_f32_e32 v36, v36, v220
	v_mul_f32_e32 v46, v207, v46
	v_mul_f32_e32 v48, v209, v48
	v_mul_f32_e32 v42, v211, v42
	v_mul_f32_e32 v44, v213, v44
	v_mul_f32_e32 v38, v215, v38
	v_mul_f32_e32 v40, v217, v40
	v_mul_f32_e32 v34, v219, v34
	v_mul_f32_e32 v36, v221, v36
	v_cvt_pk_fp8_f32 v222, v46, v48
	v_cvt_pk_fp8_f32 v223, v38, v40
	v_add_co_u32_e32 v224, vcc, 0x58000, v18
	s_nop 1
	v_addc_co_u32_e32 v225, vcc, 0, v19, vcc
	v_cvt_pk_fp8_f32 v222, v42, v44 op_sel:[0,0,1]
	v_cvt_pk_fp8_f32 v223, v34, v36 op_sel:[0,0,1]
	global_store_dwordx2 v[224:225], v[222:223], off
	s_and_b64 vcc, exec, s[0:1]
	s_mov_b64 s[0:1], -1
	s_cbranch_vccnz .LBB0_603
	s_andn2_b64 vcc, exec, s[12:13]
	s_cbranch_vccnz .LBB0_602
	s_barrier
	s_branch .LBB0_602
